# v100 + chain/share boustrophedon QK^T MFMA order in the real MoBA hot loops (the zero-initialised MODE 0 loops; earlier attention edits had hit the FoX loops)
# speedup vs baseline: 1.0018x; 1.0018x over previous
.LBB0_358:
	s_mov_b32 m0, s96
	s_add_i32 s2, s88, 0xff000000
	buffer_load_dwordx4 v175, s[64:67], s2 offen lds
	s_add_i32 s2, s88, 0xff002000
	s_mov_b32 m0, s93
	s_nop 0
	buffer_load_dwordx4 v175, s[64:67], s2 offen lds
	s_add_i32 s2, s75, s86
	s_mov_b32 m0, s2
	s_nop 0
	buffer_load_dwordx4 v182, s[64:67], s88 offen lds
	s_add_i32 m0, s2, 0x400
	s_add_i32 s2, s88, 0x80
	buffer_load_dwordx4 v182, s[64:67], s2 offen lds
	v_exp_f32_e32 v17, v146
	v_exp_f32_e32 v195, v147
	v_exp_f32_e32 v214, v152
	v_exp_f32_e32 v216, v154
	v_exp_f32_e32 v152, v156
	v_exp_f32_e32 v154, v157
	v_exp_f32_e32 v196, v148
	v_exp_f32_e32 v217, v155
	v_exp_f32_e32 v155, v158
	v_exp_f32_e32 v213, v149
	v_exp_f32_e32 v156, v159
	v_exp_f32_e32 v157, v160
	v_exp_f32_e32 v215, v153
	v_exp_f32_e32 v158, v161
	v_add_f32_e32 v2, v197, v198
	v_add_f32_e32 v4, v202, v204
	v_add_f32_e32 v5, v17, v195
	v_add_f32_e32 v6, v152, v154
	v_exp_f32_e32 v159, v162
	v_add_f32_e32 v2, v199, v2
	v_add_f32_e32 v4, v206, v4
	v_add_f32_e32 v5, v196, v5
	v_add_f32_e32 v6, v155, v6
	v_exp_f32_e32 v160, v163
	v_add_f32_e32 v2, v200, v2
	v_add_f32_e32 v4, v208, v4
	v_add_f32_e32 v5, v213, v5
	v_add_f32_e32 v6, v156, v6
	v_add_f32_e32 v2, v201, v2
	v_add_f32_e32 v4, v209, v4
	v_add_f32_e32 v5, v214, v5
	v_add_f32_e32 v6, v157, v6
	v_add_f32_e32 v2, v203, v2
	v_add_f32_e32 v4, v210, v4
	v_add_f32_e32 v5, v215, v5
	v_add_f32_e32 v6, v158, v6
	v_add_f32_e32 v2, v205, v2
	v_add_f32_e32 v4, v211, v4
	v_add_f32_e32 v5, v216, v5
	v_add_f32_e32 v6, v159, v6
	v_add_f32_e32 v2, v207, v2
	v_add_f32_e32 v4, v212, v4
	v_add_f32_e32 v5, v217, v5
	v_add_f32_e32 v6, v160, v6
	v_add_f32_e32 v2, v4, v2
	v_add_f32_e32 v4, v6, v5
	v_add_f32_e32 v2, v2, v4
	v_mov_b32_e32 v16, v2
	s_nop 1
	v_permlane32_swap_b32_e32 v2, v16
	ds_read_b128 v[4:7], v192
	ds_read_b128 v[8:11], v192 offset:8192
	ds_read_b128 v[12:15], v190 offset:8192
	ds_read_b128 v[146:149], v190
	ds_read_b128 v[218:221], v189
	ds_read_b128 v[222:225], v189 offset:8192
	ds_read_b128 v[226:229], v188 offset:8192
	ds_read_b128 v[230:233], v188
	s_waitcnt lgkmcnt(7)
	v_mfma_f32_32x32x16_bf16 v[98:113], v[4:7], v[142:145], 0
	ds_read_b128 v[4:7], v192 offset:128
	ds_read_b128 v[234:237], v192 offset:8320
	s_waitcnt lgkmcnt(8)
	v_mfma_f32_32x32x16_bf16 v[82:97], v[8:11], v[142:145], 0
	s_waitcnt lgkmcnt(7)
	v_mfma_f32_32x32x16_bf16 v[82:97], v[12:15], v[138:141], v[82:97]
	ds_read_b128 v[8:11], v190 offset:8320
	ds_read_b128 v[12:15], v190 offset:128
	s_waitcnt lgkmcnt(8)
	v_mfma_f32_32x32x16_bf16 v[98:113], v[146:149], v[138:141], v[98:113]
	s_waitcnt lgkmcnt(7)
	v_mfma_f32_32x32x16_bf16 v[98:113], v[218:221], v[134:137], v[98:113]
	ds_read_b128 v[146:149], v189 offset:128
	ds_read_b128 v[218:221], v189 offset:8320
	s_waitcnt lgkmcnt(8)
	v_mfma_f32_32x32x16_bf16 v[82:97], v[222:225], v[134:137], v[82:97]
	s_waitcnt lgkmcnt(7)
	v_mfma_f32_32x32x16_bf16 v[82:97], v[226:229], v[130:133], v[82:97]
	ds_read_b128 v[222:225], v188 offset:8320
	ds_read_b128 v[226:229], v188 offset:128
	s_waitcnt lgkmcnt(8)
	v_mfma_f32_32x32x16_bf16 v[98:113], v[230:233], v[130:133], v[98:113]
	s_waitcnt lgkmcnt(7)
	v_mfma_f32_32x32x16_bf16 v[98:113], v[4:7], v[126:129], v[98:113]
	s_waitcnt lgkmcnt(6)
	v_mfma_f32_32x32x16_bf16 v[82:97], v[234:237], v[126:129], v[82:97]
	s_waitcnt lgkmcnt(5)
	v_mfma_f32_32x32x16_bf16 v[82:97], v[8:11], v[122:125], v[82:97]
	s_waitcnt lgkmcnt(4)
	v_mfma_f32_32x32x16_bf16 v[98:113], v[12:15], v[122:125], v[98:113]
	s_waitcnt lgkmcnt(3)
	v_mfma_f32_32x32x16_bf16 v[98:113], v[146:149], v[118:121], v[98:113]
	s_waitcnt lgkmcnt(2)
	v_mfma_f32_32x32x16_bf16 v[82:97], v[218:221], v[118:121], v[82:97]
	s_waitcnt lgkmcnt(1)
	v_mfma_f32_32x32x16_bf16 v[82:97], v[222:225], v[114:117], v[82:97]
	s_waitcnt lgkmcnt(0)
	v_mfma_f32_32x32x16_bf16 v[98:113], v[226:229], v[114:117], v[98:113]
	v_add_u32_e32 v153, s4, v181
	ds_read_b64_tr_b16 v[146:147], v153 offset:0
	ds_read_b64_tr_b16 v[148:149], v153 offset:0x800
	ds_read_b64_tr_b16 v[12:13], v153 offset:0x1000
	ds_read_b64_tr_b16 v[14:15], v153 offset:0x1800
	ds_read_b64_tr_b16 v[8:9], v153 offset:0x2000
	ds_read_b64_tr_b16 v[10:11], v153 offset:0x2800
	ds_read_b64_tr_b16 v[4:5], v153 offset:0x3000
	ds_read_b64_tr_b16 v[6:7], v153 offset:0x3800
	s_sub_i32 s2, s87, 64
	s_cmp_le_i32 s2, s92
	s_cbranch_scc1 .LBB0_360
	v_add_u32_e32 v161, 64, v193
	v_cmp_gt_i32_e64 s[60:61], 26, v161
	v_cmp_gt_i32_e64 s[62:63], 27, v161
	v_cmp_gt_i32_e64 s[58:59], 25, v161
	s_and_b64 s[60:61], s[62:63], s[60:61]
	v_cmp_gt_i32_e64 s[56:57], 24, v161
	s_and_b64 s[58:59], s[60:61], s[58:59]
	v_cmp_gt_i32_e64 s[54:55], 19, v161
	s_and_b64 s[56:57], s[58:59], s[56:57]
	v_cmp_gt_i32_e64 s[52:53], 18, v161
	s_and_b64 s[54:55], s[56:57], s[54:55]
	v_cmp_gt_i32_e64 s[50:51], 17, v161
	s_and_b64 s[52:53], s[54:55], s[52:53]
	v_cmp_gt_i32_e64 s[48:49], 16, v161
	s_and_b64 s[50:51], s[52:53], s[50:51]
	v_cmp_gt_i32_e64 s[46:47], 11, v161
	s_and_b64 s[48:49], s[50:51], s[48:49]
	v_cmp_gt_i32_e64 s[44:45], 10, v161
	s_and_b64 s[46:47], s[48:49], s[46:47]
	v_cmp_gt_i32_e64 s[42:43], 9, v161
	s_and_b64 s[44:45], s[46:47], s[44:45]
	v_cmp_gt_i32_e64 s[40:41], 8, v161
	s_and_b64 s[42:43], s[44:45], s[42:43]
	v_cmp_gt_i32_e64 s[38:39], 3, v161
	s_and_b64 s[40:41], s[42:43], s[40:41]
	v_cmp_gt_i32_e64 s[36:37], 2, v161
	s_and_b64 s[38:39], s[40:41], s[38:39]
	v_cmp_gt_i32_e64 s[34:35], 1, v161
	s_and_b64 s[36:37], s[38:39], s[36:37]
	v_cmp_gt_i32_e64 s[30:31], 0, v161
	s_and_b64 s[34:35], s[36:37], s[34:35]
	s_and_b64 s[30:31], s[34:35], s[30:31]
	v_cmp_gt_i32_e64 s[28:29], 58, v161
	v_cndmask_b32_e64 v98, v98, v171, s[30:31]
	v_cmp_gt_i32_e64 s[30:31], 59, v161
	v_cmp_gt_i32_e64 s[26:27], 57, v161
	s_and_b64 s[28:29], s[30:31], s[28:29]
	v_cmp_gt_i32_e64 s[24:25], 56, v161
	s_and_b64 s[26:27], s[28:29], s[26:27]
	v_cmp_gt_i32_e64 s[22:23], 51, v161
	s_and_b64 s[24:25], s[26:27], s[24:25]
	v_cmp_gt_i32_e64 s[20:21], 50, v161
	s_and_b64 s[22:23], s[24:25], s[22:23]
	v_cmp_gt_i32_e64 s[18:19], 49, v161
	s_and_b64 s[20:21], s[22:23], s[20:21]
	v_cmp_gt_i32_e64 s[16:17], 48, v161
	s_and_b64 s[18:19], s[20:21], s[18:19]
	v_cmp_gt_i32_e64 s[14:15], 43, v161
	s_and_b64 s[16:17], s[18:19], s[16:17]
	v_cmp_gt_i32_e64 s[12:13], 42, v161
	s_and_b64 s[14:15], s[16:17], s[14:15]
	v_cmp_gt_i32_e64 s[10:11], 41, v161
	s_and_b64 s[12:13], s[14:15], s[12:13]
	v_cmp_gt_i32_e64 s[8:9], 40, v161
	s_and_b64 s[10:11], s[12:13], s[10:11]
	v_cmp_gt_i32_e64 s[6:7], 35, v161
	s_and_b64 s[8:9], s[10:11], s[8:9]
	v_cmp_gt_i32_e64 s[4:5], 34, v161
	s_and_b64 s[6:7], s[8:9], s[6:7]
	v_cmp_gt_i32_e64 s[2:3], 33, v161
	s_and_b64 s[4:5], s[6:7], s[4:5]
	v_cmp_gt_i32_e32 vcc, 32, v161
	s_and_b64 s[2:3], s[4:5], s[2:3]
	s_and_b64 vcc, s[2:3], vcc
	v_cndmask_b32_e64 v113, v113, v171, s[62:63]
	v_cndmask_b32_e64 v112, v112, v171, s[60:61]
	v_cndmask_b32_e64 v111, v111, v171, s[58:59]
	v_cndmask_b32_e64 v110, v110, v171, s[56:57]
	v_cndmask_b32_e64 v109, v109, v171, s[54:55]
	v_cndmask_b32_e64 v108, v108, v171, s[52:53]
	v_cndmask_b32_e64 v107, v107, v171, s[50:51]
	v_cndmask_b32_e64 v106, v106, v171, s[48:49]
	v_cndmask_b32_e64 v105, v105, v171, s[46:47]
	v_cndmask_b32_e64 v104, v104, v171, s[44:45]
	v_cndmask_b32_e64 v103, v103, v171, s[42:43]
	v_cndmask_b32_e64 v102, v102, v171, s[40:41]
	v_cndmask_b32_e64 v101, v101, v171, s[38:39]
	v_cndmask_b32_e64 v100, v100, v171, s[36:37]
	v_cndmask_b32_e64 v99, v99, v171, s[34:35]
	v_cndmask_b32_e64 v97, v97, v171, s[30:31]
	v_cndmask_b32_e64 v96, v96, v171, s[28:29]
	v_cndmask_b32_e64 v95, v95, v171, s[26:27]
	v_cndmask_b32_e64 v94, v94, v171, s[24:25]
	v_cndmask_b32_e64 v93, v93, v171, s[22:23]
	v_cndmask_b32_e64 v92, v92, v171, s[20:21]
	v_cndmask_b32_e64 v91, v91, v171, s[18:19]
	v_cndmask_b32_e64 v90, v90, v171, s[16:17]
	v_cndmask_b32_e64 v89, v89, v171, s[14:15]
	v_cndmask_b32_e64 v88, v88, v171, s[12:13]
	v_cndmask_b32_e64 v87, v87, v171, s[10:11]
	v_cndmask_b32_e64 v86, v86, v171, s[8:9]
	v_cndmask_b32_e64 v85, v85, v171, s[6:7]
	v_cndmask_b32_e64 v84, v84, v171, s[4:5]
	v_cndmask_b32_e64 v83, v83, v171, s[2:3]
	v_cndmask_b32_e32 v82, v82, v171, vcc

.LBB0_366:
	v_cndmask_b32_e64 v152, v152, v191, s[4:5]
	v_cndmask_b32_e64 v4, v174, v152, s[2:3]
	v_sub_f32_e32 v5, v98, v4
	v_sub_f32_e32 v6, v99, v4
	v_sub_f32_e32 v7, v100, v4
	v_sub_f32_e32 v8, v101, v4
	v_sub_f32_e32 v9, v102, v4
	v_sub_f32_e32 v10, v103, v4
	v_sub_f32_e32 v11, v104, v4
	v_sub_f32_e32 v12, v105, v4
	v_sub_f32_e32 v13, v106, v4
	v_sub_f32_e32 v14, v107, v4
	v_sub_f32_e32 v15, v108, v4
	v_sub_f32_e32 v98, v109, v4
	v_sub_f32_e32 v99, v110, v4
	v_sub_f32_e32 v100, v111, v4
	v_sub_f32_e32 v101, v112, v4
	v_sub_f32_e32 v102, v113, v4
	v_exp_f32_e32 v154, v5
	v_exp_f32_e32 v156, v6
	v_exp_f32_e32 v157, v7
	v_exp_f32_e32 v160, v8
	v_exp_f32_e32 v161, v9
	v_exp_f32_e32 v191, v10
	v_exp_f32_e32 v197, v11
	v_exp_f32_e32 v200, v12
	v_exp_f32_e32 v155, v13
	v_exp_f32_e32 v158, v14
	v_exp_f32_e32 v159, v15
	v_exp_f32_e32 v162, v98
	v_exp_f32_e32 v163, v99
	v_exp_f32_e32 v198, v100
	v_exp_f32_e32 v199, v101
	v_exp_f32_e32 v201, v102
	v_sub_f32_e32 v82, v82, v4
	v_sub_f32_e32 v83, v83, v4
	v_sub_f32_e32 v84, v84, v4
	v_sub_f32_e32 v85, v85, v4
	v_sub_f32_e32 v86, v86, v4
	v_sub_f32_e32 v87, v87, v4
	v_sub_f32_e32 v88, v88, v4
	v_sub_f32_e32 v89, v89, v4
	v_sub_f32_e32 v90, v90, v4
	v_sub_f32_e32 v91, v91, v4
	v_sub_f32_e32 v92, v92, v4
	v_sub_f32_e32 v93, v93, v4
	v_sub_f32_e32 v94, v94, v4
	v_sub_f32_e32 v5, v95, v4
	v_sub_f32_e32 v6, v96, v4
	v_sub_f32_e32 v4, v97, v4
	v_exp_f32_e32 v202, v82
	v_exp_f32_e32 v204, v83
	v_exp_f32_e32 v203, v90
	v_exp_f32_e32 v206, v91
	v_exp_f32_e32 v205, v84
	v_exp_f32_e32 v207, v92
	v_exp_f32_e32 v208, v85
	v_exp_f32_e32 v210, v93
	v_exp_f32_e32 v209, v86
	v_exp_f32_e32 v211, v94
	v_exp_f32_e32 v212, v87
	v_exp_f32_e32 v214, v5
	v_exp_f32_e32 v215, v6
	v_exp_f32_e32 v217, v4
	v_add_f32_e32 v4, v154, v156
	v_add_f32_e32 v5, v155, v158
	v_add_f32_e32 v6, v202, v204
	v_add_f32_e32 v7, v203, v206
	v_exp_f32_e32 v213, v88
	v_add_f32_e32 v4, v157, v4
	v_add_f32_e32 v5, v159, v5
	v_add_f32_e32 v6, v205, v6
	v_add_f32_e32 v7, v207, v7
	v_exp_f32_e32 v216, v89
	v_add_f32_e32 v4, v160, v4
	v_add_f32_e32 v5, v162, v5
	v_add_f32_e32 v6, v208, v6
	v_add_f32_e32 v7, v210, v7
	v_add_f32_e32 v4, v161, v4
	v_add_f32_e32 v5, v163, v5
	v_add_f32_e32 v6, v209, v6
	v_add_f32_e32 v7, v211, v7
	v_add_f32_e32 v4, v191, v4
	v_add_f32_e32 v5, v198, v5
	v_add_f32_e32 v6, v212, v6
	v_add_f32_e32 v7, v214, v7
	v_add_f32_e32 v4, v197, v4
	v_add_f32_e32 v5, v199, v5
	v_add_f32_e32 v6, v213, v6
	v_add_f32_e32 v7, v215, v7
	v_add_f32_e32 v4, v200, v4
	v_add_f32_e32 v5, v201, v5
	v_add_f32_e32 v6, v216, v6
	v_add_f32_e32 v7, v217, v7
	v_add_f32_e32 v4, v5, v4
	v_add_f32_e32 v5, v7, v6
	v_add_f32_e32 v195, v5, v4
	v_mov_b32_e32 v196, v195
	s_nop 1
	v_permlane32_swap_b32_e32 v195, v196
	ds_read_b128 v[4:7], v183 offset:49152
	ds_read_b128 v[8:11], v183 offset:57344
	ds_read_b128 v[12:15], v184 offset:57344
	ds_read_b128 v[146:149], v184 offset:49152
	ds_read_b128 v[218:221], v185 offset:49152
	ds_read_b128 v[222:225], v185 offset:57344
	ds_read_b128 v[226:229], v186 offset:57344
	ds_read_b128 v[230:233], v186 offset:49152
	s_waitcnt lgkmcnt(7)
	v_mfma_f32_32x32x16_bf16 v[98:113], v[4:7], v[142:145], 0
	ds_read_b128 v[4:7], v183 offset:49280
	ds_read_b128 v[234:237], v183 offset:57472
	s_waitcnt lgkmcnt(8)
	v_mfma_f32_32x32x16_bf16 v[82:97], v[8:11], v[142:145], 0
	s_waitcnt lgkmcnt(7)
	v_mfma_f32_32x32x16_bf16 v[82:97], v[12:15], v[138:141], v[82:97]
	ds_read_b128 v[8:11], v184 offset:57472
	ds_read_b128 v[12:15], v184 offset:49280
	s_waitcnt lgkmcnt(8)
	v_mfma_f32_32x32x16_bf16 v[98:113], v[146:149], v[138:141], v[98:113]
	s_waitcnt lgkmcnt(7)
	v_mfma_f32_32x32x16_bf16 v[98:113], v[218:221], v[134:137], v[98:113]
	ds_read_b128 v[146:149], v185 offset:49280
	ds_read_b128 v[218:221], v185 offset:57472
	s_waitcnt lgkmcnt(8)
	v_mfma_f32_32x32x16_bf16 v[82:97], v[222:225], v[134:137], v[82:97]
	s_waitcnt lgkmcnt(7)
	v_mfma_f32_32x32x16_bf16 v[82:97], v[226:229], v[130:133], v[82:97]
	ds_read_b128 v[222:225], v186 offset:57472
	ds_read_b128 v[226:229], v186 offset:49280
	s_waitcnt lgkmcnt(8)
	v_mfma_f32_32x32x16_bf16 v[98:113], v[230:233], v[130:133], v[98:113]
	s_waitcnt lgkmcnt(7)
	v_mfma_f32_32x32x16_bf16 v[98:113], v[4:7], v[126:129], v[98:113]
	s_waitcnt lgkmcnt(6)
	v_mfma_f32_32x32x16_bf16 v[82:97], v[234:237], v[126:129], v[82:97]
	s_waitcnt lgkmcnt(5)
	v_mfma_f32_32x32x16_bf16 v[82:97], v[8:11], v[122:125], v[82:97]
	s_waitcnt lgkmcnt(4)
	v_mfma_f32_32x32x16_bf16 v[98:113], v[12:15], v[122:125], v[98:113]
	s_waitcnt lgkmcnt(3)
	v_mfma_f32_32x32x16_bf16 v[98:113], v[146:149], v[118:121], v[98:113]
	s_waitcnt lgkmcnt(2)
	v_mfma_f32_32x32x16_bf16 v[82:97], v[218:221], v[118:121], v[82:97]
	s_waitcnt lgkmcnt(1)
	v_mfma_f32_32x32x16_bf16 v[82:97], v[222:225], v[114:117], v[82:97]
	s_waitcnt lgkmcnt(0)
	v_mfma_f32_32x32x16_bf16 v[98:113], v[226:229], v[114:117], v[98:113]
	v_add_u32_e32 v153, s79, v181
	ds_read_b64_tr_b16 v[146:147], v153 offset:0
	ds_read_b64_tr_b16 v[148:149], v153 offset:0x800
	ds_read_b64_tr_b16 v[12:13], v153 offset:0x1000
	ds_read_b64_tr_b16 v[14:15], v153 offset:0x1800
	ds_read_b64_tr_b16 v[8:9], v153 offset:0x2000
	ds_read_b64_tr_b16 v[10:11], v153 offset:0x2800
	ds_read_b64_tr_b16 v[4:5], v153 offset:0x3000
	ds_read_b64_tr_b16 v[6:7], v153 offset:0x3800
	s_cmp_le_i32 s87, s92
	s_cbranch_scc1 .LBB0_368
	v_cmp_gt_i32_e64 s[60:61], 26, v193
	v_cmp_gt_i32_e64 s[62:63], 27, v193
	v_cmp_gt_i32_e64 s[58:59], 25, v193
	s_and_b64 s[60:61], s[62:63], s[60:61]
	v_cmp_gt_i32_e64 s[56:57], 24, v193
	s_and_b64 s[58:59], s[60:61], s[58:59]
	v_cmp_gt_i32_e64 s[54:55], 19, v193
	s_and_b64 s[56:57], s[58:59], s[56:57]
	v_cmp_gt_i32_e64 s[52:53], 18, v193
	s_and_b64 s[54:55], s[56:57], s[54:55]
	v_cmp_gt_i32_e64 s[50:51], 17, v193
	s_and_b64 s[52:53], s[54:55], s[52:53]
	v_cmp_gt_i32_e64 s[48:49], 16, v193
	s_and_b64 s[50:51], s[52:53], s[50:51]
	v_cmp_gt_i32_e64 s[46:47], 11, v193
	s_and_b64 s[48:49], s[50:51], s[48:49]
	v_cmp_gt_i32_e64 s[44:45], 10, v193
	s_and_b64 s[46:47], s[48:49], s[46:47]
	v_cmp_gt_i32_e64 s[42:43], 9, v193
	s_and_b64 s[44:45], s[46:47], s[44:45]
	v_cmp_gt_i32_e64 s[40:41], 8, v193
	s_and_b64 s[42:43], s[44:45], s[42:43]
	v_cmp_gt_i32_e64 s[38:39], 3, v193
	s_and_b64 s[40:41], s[42:43], s[40:41]
	v_cmp_gt_i32_e64 s[36:37], 2, v193
	s_and_b64 s[38:39], s[40:41], s[38:39]
	v_cmp_gt_i32_e64 s[34:35], 1, v193
	s_and_b64 s[36:37], s[38:39], s[36:37]
	v_cmp_gt_i32_e64 s[30:31], 0, v193
	s_and_b64 s[34:35], s[36:37], s[34:35]
	s_and_b64 s[30:31], s[34:35], s[30:31]
	v_cmp_gt_i32_e64 s[28:29], 58, v193
	v_cndmask_b32_e64 v98, v98, v171, s[30:31]
	v_cmp_gt_i32_e64 s[30:31], 59, v193
	v_cmp_gt_i32_e64 s[26:27], 57, v193
	s_and_b64 s[28:29], s[30:31], s[28:29]
	v_cmp_gt_i32_e64 s[24:25], 56, v193
	s_and_b64 s[26:27], s[28:29], s[26:27]
	v_cmp_gt_i32_e64 s[22:23], 51, v193
	s_and_b64 s[24:25], s[26:27], s[24:25]
	v_cmp_gt_i32_e64 s[20:21], 50, v193
	s_and_b64 s[22:23], s[24:25], s[22:23]
	v_cmp_gt_i32_e64 s[18:19], 49, v193
	s_and_b64 s[20:21], s[22:23], s[20:21]
	v_cmp_gt_i32_e64 s[16:17], 48, v193
	s_and_b64 s[18:19], s[20:21], s[18:19]
	v_cmp_gt_i32_e64 s[14:15], 43, v193
	s_and_b64 s[16:17], s[18:19], s[16:17]
	v_cmp_gt_i32_e64 s[12:13], 42, v193
	s_and_b64 s[14:15], s[16:17], s[14:15]
	v_cmp_gt_i32_e64 s[10:11], 41, v193
	s_and_b64 s[12:13], s[14:15], s[12:13]
	v_cmp_gt_i32_e64 s[8:9], 40, v193
	s_and_b64 s[10:11], s[12:13], s[10:11]
	v_cmp_gt_i32_e64 s[6:7], 35, v193
	s_and_b64 s[8:9], s[10:11], s[8:9]
	v_cmp_gt_i32_e64 s[4:5], 34, v193
	s_and_b64 s[6:7], s[8:9], s[6:7]
	v_cmp_gt_i32_e64 s[2:3], 33, v193
	s_and_b64 s[4:5], s[6:7], s[4:5]
	v_cmp_gt_i32_e32 vcc, 32, v193
	s_and_b64 s[2:3], s[4:5], s[2:3]
	s_and_b64 vcc, s[2:3], vcc
	v_cndmask_b32_e64 v113, v113, v171, s[62:63]
	v_cndmask_b32_e64 v112, v112, v171, s[60:61]
	v_cndmask_b32_e64 v111, v111, v171, s[58:59]
	v_cndmask_b32_e64 v110, v110, v171, s[56:57]
	v_cndmask_b32_e64 v109, v109, v171, s[54:55]
	v_cndmask_b32_e64 v108, v108, v171, s[52:53]
	v_cndmask_b32_e64 v107, v107, v171, s[50:51]
	v_cndmask_b32_e64 v106, v106, v171, s[48:49]
	v_cndmask_b32_e64 v105, v105, v171, s[46:47]
	v_cndmask_b32_e64 v104, v104, v171, s[44:45]
	v_cndmask_b32_e64 v103, v103, v171, s[42:43]
	v_cndmask_b32_e64 v102, v102, v171, s[40:41]
	v_cndmask_b32_e64 v101, v101, v171, s[38:39]
	v_cndmask_b32_e64 v100, v100, v171, s[36:37]
	v_cndmask_b32_e64 v99, v99, v171, s[34:35]
	v_cndmask_b32_e64 v97, v97, v171, s[30:31]
	v_cndmask_b32_e64 v96, v96, v171, s[28:29]
	v_cndmask_b32_e64 v95, v95, v171, s[26:27]
	v_cndmask_b32_e64 v94, v94, v171, s[24:25]
	v_cndmask_b32_e64 v93, v93, v171, s[22:23]
	v_cndmask_b32_e64 v92, v92, v171, s[20:21]
	v_cndmask_b32_e64 v91, v91, v171, s[18:19]
	v_cndmask_b32_e64 v90, v90, v171, s[16:17]
	v_cndmask_b32_e64 v89, v89, v171, s[14:15]
	v_cndmask_b32_e64 v88, v88, v171, s[12:13]
	v_cndmask_b32_e64 v87, v87, v171, s[10:11]
	v_cndmask_b32_e64 v86, v86, v171, s[8:9]
	v_cndmask_b32_e64 v85, v85, v171, s[6:7]
	v_cndmask_b32_e64 v84, v84, v171, s[4:5]
	v_cndmask_b32_e64 v83, v83, v171, s[2:3]
	v_cndmask_b32_e32 v82, v82, v171, vcc

.LBB0_393:
	s_mov_b32 m0, s92
	s_add_i32 s2, s88, 0xff000000
	buffer_load_dwordx4 v175, s[64:67], s2 offen lds
	s_add_i32 s2, s88, 0xff002000
	s_mov_b32 m0, s71
	s_nop 0
	buffer_load_dwordx4 v175, s[64:67], s2 offen lds
	s_add_i32 s2, s95, s86
	s_mov_b32 m0, s2
	s_nop 0
	buffer_load_dwordx4 v182, s[64:67], s88 offen lds
	s_add_i32 m0, s2, 0x400
	s_add_i32 s2, s88, 0x80
	buffer_load_dwordx4 v182, s[64:67], s2 offen lds
	ds_read_b128 v[4:7], v192
	ds_read_b128 v[8:11], v192 offset:8192
	ds_read_b128 v[12:15], v191 offset:8192
	ds_read_b128 v[212:215], v191
	ds_read_b128 v[216:219], v190
	ds_read_b128 v[220:223], v190 offset:8192
	ds_read_b128 v[224:227], v189 offset:8192
	ds_read_b128 v[228:231], v189
	s_waitcnt lgkmcnt(7)
	v_mfma_f32_32x32x16_bf16 v[98:113], v[4:7], v[142:145], 0
	ds_read_b128 v[4:7], v192 offset:128
	ds_read_b128 v[232:235], v192 offset:8320
	s_waitcnt lgkmcnt(8)
	v_mfma_f32_32x32x16_bf16 v[82:97], v[8:11], v[142:145], 0
	s_waitcnt lgkmcnt(7)
	v_mfma_f32_32x32x16_bf16 v[82:97], v[12:15], v[138:141], v[82:97]
	ds_read_b128 v[8:11], v191 offset:8320
	ds_read_b128 v[12:15], v191 offset:128
	s_waitcnt lgkmcnt(8)
	v_mfma_f32_32x32x16_bf16 v[98:113], v[212:215], v[138:141], v[98:113]
	s_waitcnt lgkmcnt(7)
	v_mfma_f32_32x32x16_bf16 v[98:113], v[216:219], v[134:137], v[98:113]
	ds_read_b128 v[212:215], v190 offset:128
	ds_read_b128 v[216:219], v190 offset:8320
	s_waitcnt lgkmcnt(8)
	v_mfma_f32_32x32x16_bf16 v[82:97], v[220:223], v[134:137], v[82:97]
	s_waitcnt lgkmcnt(7)
	v_mfma_f32_32x32x16_bf16 v[82:97], v[224:227], v[130:133], v[82:97]
	ds_read_b128 v[220:223], v189 offset:8320
	ds_read_b128 v[224:227], v189 offset:128
	s_waitcnt lgkmcnt(8)
	v_mfma_f32_32x32x16_bf16 v[98:113], v[228:231], v[130:133], v[98:113]
	s_waitcnt lgkmcnt(7)
	v_mfma_f32_32x32x16_bf16 v[98:113], v[4:7], v[126:129], v[98:113]
	s_waitcnt lgkmcnt(6)
	v_mfma_f32_32x32x16_bf16 v[82:97], v[232:235], v[126:129], v[82:97]
	s_waitcnt lgkmcnt(5)
	v_mfma_f32_32x32x16_bf16 v[82:97], v[8:11], v[122:125], v[82:97]
	s_waitcnt lgkmcnt(4)
	v_mfma_f32_32x32x16_bf16 v[98:113], v[12:15], v[122:125], v[98:113]
	s_waitcnt lgkmcnt(3)
	v_mfma_f32_32x32x16_bf16 v[98:113], v[212:215], v[118:121], v[98:113]
	s_waitcnt lgkmcnt(2)
	v_mfma_f32_32x32x16_bf16 v[82:97], v[216:219], v[118:121], v[82:97]
	s_waitcnt lgkmcnt(1)
	v_mfma_f32_32x32x16_bf16 v[82:97], v[220:223], v[114:117], v[82:97]
	s_waitcnt lgkmcnt(0)
	v_mfma_f32_32x32x16_bf16 v[98:113], v[224:227], v[114:117], v[98:113]
	v_exp_f32_e32 v211, v148
	v_exp_f32_e32 v216, v149
	v_exp_f32_e32 v223, v156
	v_exp_f32_e32 v224, v157
	v_exp_f32_e32 v217, v150
	v_exp_f32_e32 v225, v158
	v_exp_f32_e32 v218, v151
	v_exp_f32_e32 v226, v159
	v_exp_f32_e32 v219, v152
	v_exp_f32_e32 v227, v160
	v_exp_f32_e32 v220, v153
	v_exp_f32_e32 v228, v161
	v_add_f32_e32 v2, v195, v196
	v_add_f32_e32 v4, v200, v202
	v_add_f32_e32 v148, v211, v216
	v_add_f32_e32 v149, v223, v224
	v_add_u32_e32 v5, s4, v181
	ds_read_b64_tr_b16 v[6:7], v5 offset:0
	v_exp_f32_e32 v221, v154
	v_exp_f32_e32 v229, v162
	v_add_f32_e32 v2, v197, v2
	v_add_f32_e32 v4, v204, v4
	v_add_f32_e32 v148, v217, v148
	v_add_f32_e32 v149, v225, v149
	ds_read_b64_tr_b16 v[8:9], v5 offset:0x800
	v_exp_f32_e32 v222, v155
	v_exp_f32_e32 v163, v163
	v_add_f32_e32 v2, v198, v2
	v_add_f32_e32 v4, v206, v4
	v_add_f32_e32 v148, v218, v148
	v_add_f32_e32 v149, v226, v149
	ds_read_b64_tr_b16 v[10:11], v5 offset:0x1000
	v_add_f32_e32 v2, v199, v2
	v_add_f32_e32 v4, v207, v4
	v_add_f32_e32 v148, v219, v148
	v_add_f32_e32 v149, v227, v149
	ds_read_b64_tr_b16 v[12:13], v5 offset:0x1800
	v_add_f32_e32 v2, v201, v2
	v_add_f32_e32 v4, v208, v4
	v_add_f32_e32 v148, v220, v148
	v_add_f32_e32 v149, v228, v149
	ds_read_b64_tr_b16 v[14:15], v5 offset:0x2000
	v_add_f32_e32 v2, v203, v2
	v_add_f32_e32 v4, v209, v4
	v_add_f32_e32 v148, v221, v148
	v_add_f32_e32 v149, v229, v149
	ds_read_b64_tr_b16 v[16:17], v5 offset:0x2800
	v_add_f32_e32 v2, v205, v2
	v_add_f32_e32 v4, v210, v4
	v_add_f32_e32 v148, v222, v148
	v_add_f32_e32 v149, v163, v149
	ds_read_b64_tr_b16 v[212:213], v5 offset:0x3000
	v_add_f32_e32 v2, v4, v2
	v_add_f32_e32 v4, v149, v148
	ds_read_b64_tr_b16 v[214:215], v5 offset:0x3800
	v_add_f32_e32 v2, v2, v4
	v_mov_b32_e32 v4, v2
	s_nop 1
	v_permlane32_swap_b32_e32 v2, v4
	v_cvt_pk_bf16_f32 v148, v195, v196
	v_cvt_pk_bf16_f32 v149, v197, v198
	v_cvt_pk_bf16_f32 v150, v199, v201
	v_cvt_pk_bf16_f32 v151, v203, v205
	v_cvt_pk_bf16_f32 v152, v200, v202
	v_cvt_pk_bf16_f32 v153, v204, v206
	v_cvt_pk_bf16_f32 v154, v207, v208
	v_cvt_pk_bf16_f32 v155, v209, v210
	v_cvt_pk_bf16_f32 v156, v211, v216
	v_cvt_pk_bf16_f32 v157, v217, v218
	v_cvt_pk_bf16_f32 v158, v219, v220
	v_cvt_pk_bf16_f32 v159, v221, v222
	v_cvt_pk_bf16_f32 v160, v223, v224
	v_cvt_pk_bf16_f32 v161, v225, v226
	v_cvt_pk_bf16_f32 v162, v227, v228
	v_cvt_pk_bf16_f32 v163, v229, v163
	ds_read_b64_tr_b16 v[196:197], v5 offset:0x200
	ds_read_b64_tr_b16 v[198:199], v5 offset:0xa00
	ds_read_b64_tr_b16 v[200:201], v5 offset:0x1200
	ds_read_b64_tr_b16 v[202:203], v5 offset:0x1a00
	ds_read_b64_tr_b16 v[204:205], v5 offset:0x2200
	ds_read_b64_tr_b16 v[206:207], v5 offset:0x2a00
	ds_read_b64_tr_b16 v[208:209], v5 offset:0x3200
	ds_read_b64_tr_b16 v[210:211], v5 offset:0x3a00
	s_waitcnt lgkmcnt(8)
	v_mfma_f32_32x32x16_bf16 v[66:81], v[148:151], v[6:9], v[66:81]
	v_mfma_f32_32x32x16_bf16 v[66:81], v[152:155], v[10:13], v[66:81]
	v_mfma_f32_32x32x16_bf16 v[66:81], v[156:159], v[14:17], v[66:81]
	v_mfma_f32_32x32x16_bf16 v[66:81], v[160:163], v[212:215], v[66:81]
	ds_read_b64_tr_b16 v[6:7], v5 offset:0x400
	ds_read_b64_tr_b16 v[8:9], v5 offset:0xc00
	ds_read_b64_tr_b16 v[10:11], v5 offset:0x1400
	ds_read_b64_tr_b16 v[12:13], v5 offset:0x1c00
	ds_read_b64_tr_b16 v[14:15], v5 offset:0x2400
	ds_read_b64_tr_b16 v[16:17], v5 offset:0x2c00
	ds_read_b64_tr_b16 v[212:213], v5 offset:0x3400
	ds_read_b64_tr_b16 v[214:215], v5 offset:0x3c00
	s_waitcnt lgkmcnt(8)
	v_mfma_f32_32x32x16_bf16 v[50:65], v[148:151], v[196:199], v[50:65]
	v_mfma_f32_32x32x16_bf16 v[50:65], v[152:155], v[200:203], v[50:65]
	v_mfma_f32_32x32x16_bf16 v[50:65], v[156:159], v[204:207], v[50:65]
	v_mfma_f32_32x32x16_bf16 v[50:65], v[160:163], v[208:211], v[50:65]
	ds_read_b64_tr_b16 v[196:197], v5 offset:0x600
	ds_read_b64_tr_b16 v[198:199], v5 offset:0xe00
	ds_read_b64_tr_b16 v[200:201], v5 offset:0x1600
	ds_read_b64_tr_b16 v[202:203], v5 offset:0x1e00
	ds_read_b64_tr_b16 v[204:205], v5 offset:0x2600
	ds_read_b64_tr_b16 v[206:207], v5 offset:0x2e00
	ds_read_b64_tr_b16 v[208:209], v5 offset:0x3600
	ds_read_b64_tr_b16 v[210:211], v5 offset:0x3e00
	s_waitcnt lgkmcnt(8)
	v_mfma_f32_32x32x16_bf16 v[34:49], v[148:151], v[6:9], v[34:49]
	v_mfma_f32_32x32x16_bf16 v[34:49], v[152:155], v[10:13], v[34:49]
	v_mfma_f32_32x32x16_bf16 v[34:49], v[156:159], v[14:17], v[34:49]
	v_mfma_f32_32x32x16_bf16 v[34:49], v[160:163], v[212:215], v[34:49]
	s_waitcnt lgkmcnt(0)
	v_mfma_f32_32x32x16_bf16 v[18:33], v[148:151], v[196:199], v[18:33]
	s_sub_i32 s2, s87, 64
	s_cmp_le_i32 s2, s70
	v_mfma_f32_32x32x16_bf16 v[18:33], v[152:155], v[200:203], v[18:33]
	v_mfma_f32_32x32x16_bf16 v[18:33], v[156:159], v[204:207], v[18:33]
	v_mfma_f32_32x32x16_bf16 v[18:33], v[160:163], v[208:211], v[18:33]
	s_cbranch_scc1 .LBB0_395
	v_add_u32_e32 v5, 64, v193
	v_cmp_gt_i32_e64 s[60:61], 26, v5
	v_cmp_gt_i32_e64 s[62:63], 27, v5
	v_cmp_gt_i32_e64 s[58:59], 25, v5
	s_and_b64 s[60:61], s[62:63], s[60:61]
	v_cmp_gt_i32_e64 s[56:57], 24, v5
	s_and_b64 s[58:59], s[60:61], s[58:59]
	v_cmp_gt_i32_e64 s[54:55], 19, v5
	s_and_b64 s[56:57], s[58:59], s[56:57]
	v_cmp_gt_i32_e64 s[52:53], 18, v5
	s_and_b64 s[54:55], s[56:57], s[54:55]
	v_cmp_gt_i32_e64 s[50:51], 17, v5
	s_and_b64 s[52:53], s[54:55], s[52:53]
	v_cmp_gt_i32_e64 s[48:49], 16, v5
	s_and_b64 s[50:51], s[52:53], s[50:51]
	v_cmp_gt_i32_e64 s[46:47], 11, v5
	s_and_b64 s[48:49], s[50:51], s[48:49]
	v_cmp_gt_i32_e64 s[44:45], 10, v5
	s_and_b64 s[46:47], s[48:49], s[46:47]
	v_cmp_gt_i32_e64 s[42:43], 9, v5
	s_and_b64 s[44:45], s[46:47], s[44:45]
	v_cmp_gt_i32_e64 s[40:41], 8, v5
	s_and_b64 s[42:43], s[44:45], s[42:43]
	v_cmp_gt_i32_e64 s[38:39], 3, v5
	s_and_b64 s[40:41], s[42:43], s[40:41]
	v_cmp_gt_i32_e64 s[36:37], 2, v5
	s_and_b64 s[38:39], s[40:41], s[38:39]
	v_cmp_gt_i32_e64 s[34:35], 1, v5
	s_and_b64 s[36:37], s[38:39], s[36:37]
	v_cmp_gt_i32_e64 s[30:31], 0, v5
	s_and_b64 s[34:35], s[36:37], s[34:35]
	s_and_b64 s[30:31], s[34:35], s[30:31]
	v_cmp_gt_i32_e64 s[28:29], 58, v5
	v_cndmask_b32_e64 v98, v98, v171, s[30:31]
	v_cmp_gt_i32_e64 s[30:31], 59, v5
	v_cmp_gt_i32_e64 s[26:27], 57, v5
	s_and_b64 s[28:29], s[30:31], s[28:29]
	v_cmp_gt_i32_e64 s[24:25], 56, v5
	s_and_b64 s[26:27], s[28:29], s[26:27]
	v_cmp_gt_i32_e64 s[22:23], 51, v5
	s_and_b64 s[24:25], s[26:27], s[24:25]
	v_cmp_gt_i32_e64 s[20:21], 50, v5
	s_and_b64 s[22:23], s[24:25], s[22:23]
	v_cmp_gt_i32_e64 s[18:19], 49, v5
	s_and_b64 s[20:21], s[22:23], s[20:21]
	v_cmp_gt_i32_e64 s[16:17], 48, v5
	s_and_b64 s[18:19], s[20:21], s[18:19]
	v_cmp_gt_i32_e64 s[14:15], 43, v5
	s_and_b64 s[16:17], s[18:19], s[16:17]
	v_cmp_gt_i32_e64 s[12:13], 42, v5
	s_and_b64 s[14:15], s[16:17], s[14:15]
	v_cmp_gt_i32_e64 s[10:11], 41, v5
	s_and_b64 s[12:13], s[14:15], s[12:13]
	v_cmp_gt_i32_e64 s[8:9], 40, v5
	s_and_b64 s[10:11], s[12:13], s[10:11]
	v_cmp_gt_i32_e64 s[6:7], 35, v5
	s_and_b64 s[8:9], s[10:11], s[8:9]
	v_cmp_gt_i32_e64 s[4:5], 34, v5
	s_and_b64 s[6:7], s[8:9], s[6:7]
	v_cmp_gt_i32_e64 s[2:3], 33, v5
	s_and_b64 s[4:5], s[6:7], s[4:5]
	v_cmp_gt_i32_e32 vcc, 32, v5
	s_and_b64 s[2:3], s[4:5], s[2:3]
	s_and_b64 vcc, s[2:3], vcc
	v_cndmask_b32_e64 v113, v113, v171, s[62:63]
	v_cndmask_b32_e64 v112, v112, v171, s[60:61]
	v_cndmask_b32_e64 v111, v111, v171, s[58:59]
	v_cndmask_b32_e64 v110, v110, v171, s[56:57]
	v_cndmask_b32_e64 v109, v109, v171, s[54:55]
	v_cndmask_b32_e64 v108, v108, v171, s[52:53]
	v_cndmask_b32_e64 v107, v107, v171, s[50:51]
	v_cndmask_b32_e64 v106, v106, v171, s[48:49]
	v_cndmask_b32_e64 v105, v105, v171, s[46:47]
	v_cndmask_b32_e64 v104, v104, v171, s[44:45]
	v_cndmask_b32_e64 v103, v103, v171, s[42:43]
	v_cndmask_b32_e64 v102, v102, v171, s[40:41]
	v_cndmask_b32_e64 v101, v101, v171, s[38:39]
	v_cndmask_b32_e64 v100, v100, v171, s[36:37]
	v_cndmask_b32_e64 v99, v99, v171, s[34:35]
	v_cndmask_b32_e64 v97, v97, v171, s[30:31]
	v_cndmask_b32_e64 v96, v96, v171, s[28:29]
	v_cndmask_b32_e64 v95, v95, v171, s[26:27]
	v_cndmask_b32_e64 v94, v94, v171, s[24:25]
	v_cndmask_b32_e64 v93, v93, v171, s[22:23]
	v_cndmask_b32_e64 v92, v92, v171, s[20:21]
	v_cndmask_b32_e64 v91, v91, v171, s[18:19]
	v_cndmask_b32_e64 v90, v90, v171, s[16:17]
	v_cndmask_b32_e64 v89, v89, v171, s[14:15]
	v_cndmask_b32_e64 v88, v88, v171, s[12:13]
	v_cndmask_b32_e64 v87, v87, v171, s[10:11]
	v_cndmask_b32_e64 v86, v86, v171, s[8:9]
	v_cndmask_b32_e64 v85, v85, v171, s[6:7]
	v_cndmask_b32_e64 v84, v84, v171, s[4:5]
	v_cndmask_b32_e64 v83, v83, v171, s[2:3]
	v_cndmask_b32_e32 v82, v82, v171, vcc

.LBB0_401:
	v_cndmask_b32_e64 v7, v5, v188, s[4:5]
	v_cndmask_b32_e64 v5, v174, v7, s[2:3]
	v_sub_f32_e32 v8, v98, v5
	v_sub_f32_e32 v9, v99, v5
	v_sub_f32_e32 v10, v100, v5
	v_sub_f32_e32 v11, v101, v5
	v_sub_f32_e32 v12, v102, v5
	v_sub_f32_e32 v13, v103, v5
	v_sub_f32_e32 v14, v104, v5
	v_sub_f32_e32 v15, v105, v5
	v_sub_f32_e32 v16, v106, v5
	v_sub_f32_e32 v17, v107, v5
	v_sub_f32_e32 v98, v108, v5
	v_sub_f32_e32 v99, v109, v5
	v_sub_f32_e32 v100, v110, v5
	v_sub_f32_e32 v101, v111, v5
	v_sub_f32_e32 v102, v112, v5
	v_sub_f32_e32 v103, v113, v5
	v_sub_f32_e32 v188, v82, v5
	v_sub_f32_e32 v195, v83, v5
	v_sub_f32_e32 v208, v84, v5
	v_sub_f32_e32 v209, v85, v5
	v_sub_f32_e32 v210, v86, v5
	v_sub_f32_e32 v211, v87, v5
	v_sub_f32_e32 v212, v88, v5
	v_sub_f32_e32 v213, v89, v5
	v_sub_f32_e32 v214, v90, v5
	v_sub_f32_e32 v215, v91, v5
	v_sub_f32_e32 v216, v92, v5
	v_sub_f32_e32 v217, v93, v5
	v_sub_f32_e32 v218, v94, v5
	v_exp_f32_e32 v219, v8
	v_exp_f32_e32 v220, v9
	v_exp_f32_e32 v221, v10
	v_exp_f32_e32 v222, v11
	v_exp_f32_e32 v223, v12
	v_exp_f32_e32 v224, v13
	v_exp_f32_e32 v225, v14
	v_exp_f32_e32 v226, v15
	v_exp_f32_e32 v227, v16
	v_exp_f32_e32 v228, v17
	v_exp_f32_e32 v229, v98
	v_exp_f32_e32 v230, v99
	v_exp_f32_e32 v231, v100
	v_exp_f32_e32 v232, v101
	v_exp_f32_e32 v233, v102
	v_exp_f32_e32 v234, v103
	v_sub_f32_e32 v235, v95, v5
	v_sub_f32_e32 v236, v96, v5
	v_sub_f32_e32 v5, v97, v5
	ds_read_b128 v[8:11], v183 offset:49152
	ds_read_b128 v[12:15], v183 offset:57344
	ds_read_b128 v[148:151], v184 offset:57344
	ds_read_b128 v[152:155], v184 offset:49152
	ds_read_b128 v[156:159], v185 offset:49152
	ds_read_b128 v[160:163], v185 offset:57344
	ds_read_b128 v[196:199], v186 offset:57344
	ds_read_b128 v[200:203], v186 offset:49152
	s_waitcnt lgkmcnt(7)
	v_mfma_f32_32x32x16_bf16 v[98:113], v[8:11], v[142:145], 0
	ds_read_b128 v[8:11], v183 offset:49280
	ds_read_b128 v[204:207], v183 offset:57472
	s_waitcnt lgkmcnt(8)
	v_mfma_f32_32x32x16_bf16 v[82:97], v[12:15], v[142:145], 0
	s_waitcnt lgkmcnt(7)
	v_mfma_f32_32x32x16_bf16 v[82:97], v[148:151], v[138:141], v[82:97]
	ds_read_b128 v[12:15], v184 offset:57472
	ds_read_b128 v[148:151], v184 offset:49280
	s_waitcnt lgkmcnt(8)
	v_mfma_f32_32x32x16_bf16 v[98:113], v[152:155], v[138:141], v[98:113]
	s_waitcnt lgkmcnt(7)
	v_mfma_f32_32x32x16_bf16 v[98:113], v[156:159], v[134:137], v[98:113]
	ds_read_b128 v[152:155], v185 offset:49280
	ds_read_b128 v[156:159], v185 offset:57472
	s_waitcnt lgkmcnt(8)
	v_mfma_f32_32x32x16_bf16 v[82:97], v[160:163], v[134:137], v[82:97]
	s_waitcnt lgkmcnt(7)
	v_mfma_f32_32x32x16_bf16 v[82:97], v[196:199], v[130:133], v[82:97]
	ds_read_b128 v[160:163], v186 offset:57472
	ds_read_b128 v[196:199], v186 offset:49280
	s_waitcnt lgkmcnt(8)
	v_mfma_f32_32x32x16_bf16 v[98:113], v[200:203], v[130:133], v[98:113]
	s_waitcnt lgkmcnt(7)
	v_mfma_f32_32x32x16_bf16 v[98:113], v[8:11], v[126:129], v[98:113]
	s_waitcnt lgkmcnt(6)
	v_mfma_f32_32x32x16_bf16 v[82:97], v[204:207], v[126:129], v[82:97]
	s_waitcnt lgkmcnt(5)
	v_mfma_f32_32x32x16_bf16 v[82:97], v[12:15], v[122:125], v[82:97]
	s_waitcnt lgkmcnt(4)
	v_mfma_f32_32x32x16_bf16 v[98:113], v[148:151], v[122:125], v[98:113]
	s_waitcnt lgkmcnt(3)
	v_mfma_f32_32x32x16_bf16 v[98:113], v[152:155], v[118:121], v[98:113]
	s_waitcnt lgkmcnt(2)
	v_mfma_f32_32x32x16_bf16 v[82:97], v[156:159], v[118:121], v[82:97]
	s_waitcnt lgkmcnt(1)
	v_mfma_f32_32x32x16_bf16 v[82:97], v[160:163], v[114:117], v[82:97]
	s_waitcnt lgkmcnt(0)
	v_mfma_f32_32x32x16_bf16 v[98:113], v[196:199], v[114:117], v[98:113]
	v_exp_f32_e32 v188, v188
	v_exp_f32_e32 v195, v195
	v_exp_f32_e32 v203, v214
	v_exp_f32_e32 v204, v215
	v_exp_f32_e32 v197, v208
	v_exp_f32_e32 v205, v216
	v_exp_f32_e32 v198, v209
	v_exp_f32_e32 v206, v217
	v_exp_f32_e32 v199, v210
	v_exp_f32_e32 v207, v218
	v_exp_f32_e32 v200, v211
	v_exp_f32_e32 v208, v235
	v_add_f32_e32 v8, v219, v220
	v_add_f32_e32 v9, v227, v228
	v_add_f32_e32 v156, v188, v195
	v_add_f32_e32 v157, v203, v204
	v_add_u32_e32 v237, s75, v181
	ds_read_b64_tr_b16 v[10:11], v237 offset:0
	v_exp_f32_e32 v201, v212
	v_exp_f32_e32 v209, v236
	v_add_f32_e32 v8, v221, v8
	v_add_f32_e32 v9, v229, v9
	v_add_f32_e32 v156, v197, v156
	v_add_f32_e32 v157, v205, v157
	ds_read_b64_tr_b16 v[12:13], v237 offset:0x800
	v_exp_f32_e32 v202, v213
	v_exp_f32_e32 v5, v5
	v_add_f32_e32 v8, v222, v8
	v_add_f32_e32 v9, v230, v9
	v_add_f32_e32 v156, v198, v156
	v_add_f32_e32 v157, v206, v157
	ds_read_b64_tr_b16 v[14:15], v237 offset:0x1000
	v_add_f32_e32 v8, v223, v8
	v_add_f32_e32 v9, v231, v9
	v_add_f32_e32 v156, v199, v156
	v_add_f32_e32 v157, v207, v157
	ds_read_b64_tr_b16 v[16:17], v237 offset:0x1800
	v_add_f32_e32 v8, v224, v8
	v_add_f32_e32 v9, v232, v9
	v_add_f32_e32 v156, v200, v156
	v_add_f32_e32 v157, v208, v157
	ds_read_b64_tr_b16 v[148:149], v237 offset:0x2000
	v_add_f32_e32 v8, v225, v8
	v_add_f32_e32 v9, v233, v9
	v_add_f32_e32 v156, v201, v156
	v_add_f32_e32 v157, v209, v157
	ds_read_b64_tr_b16 v[150:151], v237 offset:0x2800
	v_add_f32_e32 v8, v226, v8
	v_add_f32_e32 v9, v234, v9
	v_add_f32_e32 v156, v202, v156
	v_add_f32_e32 v157, v5, v157
	ds_read_b64_tr_b16 v[152:153], v237 offset:0x3000
	v_add_f32_e32 v8, v9, v8
	v_add_f32_e32 v9, v157, v156
	ds_read_b64_tr_b16 v[154:155], v237 offset:0x3800
	v_add_f32_e32 v8, v9, v8
	v_mov_b32_e32 v9, v8
	s_nop 1
	v_permlane32_swap_b32_e32 v8, v9
	v_cvt_pk_bf16_f32 v156, v219, v220
	v_cvt_pk_bf16_f32 v157, v221, v222
	v_cvt_pk_bf16_f32 v158, v223, v224
	v_cvt_pk_bf16_f32 v159, v225, v226
	v_cvt_pk_bf16_f32 v160, v227, v228
	v_cvt_pk_bf16_f32 v161, v229, v230
	v_cvt_pk_bf16_f32 v162, v231, v232
	v_cvt_pk_bf16_f32 v163, v233, v234
	v_cvt_pk_bf16_f32 v196, v188, v195
	v_cvt_pk_bf16_f32 v197, v197, v198
	v_cvt_pk_bf16_f32 v198, v199, v200
	v_cvt_pk_bf16_f32 v199, v201, v202
	v_cvt_pk_bf16_f32 v200, v203, v204
	v_cvt_pk_bf16_f32 v201, v205, v206
	v_cvt_pk_bf16_f32 v202, v207, v208
	v_cvt_pk_bf16_f32 v203, v209, v5
	ds_read_b64_tr_b16 v[204:205], v237 offset:0x200
	ds_read_b64_tr_b16 v[206:207], v237 offset:0xa00
	ds_read_b64_tr_b16 v[208:209], v237 offset:0x1200
	ds_read_b64_tr_b16 v[210:211], v237 offset:0x1a00
	ds_read_b64_tr_b16 v[212:213], v237 offset:0x2200
	ds_read_b64_tr_b16 v[214:215], v237 offset:0x2a00
	ds_read_b64_tr_b16 v[216:217], v237 offset:0x3200
	ds_read_b64_tr_b16 v[218:219], v237 offset:0x3a00
	s_waitcnt lgkmcnt(8)
	v_mfma_f32_32x32x16_bf16 v[66:81], v[156:159], v[10:13], v[66:81]
	v_mfma_f32_32x32x16_bf16 v[66:81], v[160:163], v[14:17], v[66:81]
	v_mfma_f32_32x32x16_bf16 v[66:81], v[196:199], v[148:151], v[66:81]
	v_mfma_f32_32x32x16_bf16 v[66:81], v[200:203], v[152:155], v[66:81]
	ds_read_b64_tr_b16 v[10:11], v237 offset:0x400
	ds_read_b64_tr_b16 v[12:13], v237 offset:0xc00
	ds_read_b64_tr_b16 v[14:15], v237 offset:0x1400
	ds_read_b64_tr_b16 v[16:17], v237 offset:0x1c00
	ds_read_b64_tr_b16 v[148:149], v237 offset:0x2400
	ds_read_b64_tr_b16 v[150:151], v237 offset:0x2c00
	ds_read_b64_tr_b16 v[152:153], v237 offset:0x3400
	ds_read_b64_tr_b16 v[154:155], v237 offset:0x3c00
	s_waitcnt lgkmcnt(8)
	v_mfma_f32_32x32x16_bf16 v[50:65], v[156:159], v[204:207], v[50:65]
	v_mfma_f32_32x32x16_bf16 v[50:65], v[160:163], v[208:211], v[50:65]
	v_mfma_f32_32x32x16_bf16 v[50:65], v[196:199], v[212:215], v[50:65]
	v_mfma_f32_32x32x16_bf16 v[50:65], v[200:203], v[216:219], v[50:65]
	ds_read_b64_tr_b16 v[204:205], v237 offset:0x600
	ds_read_b64_tr_b16 v[206:207], v237 offset:0xe00
	ds_read_b64_tr_b16 v[208:209], v237 offset:0x1600
	ds_read_b64_tr_b16 v[210:211], v237 offset:0x1e00
	ds_read_b64_tr_b16 v[212:213], v237 offset:0x2600
	ds_read_b64_tr_b16 v[214:215], v237 offset:0x2e00
	ds_read_b64_tr_b16 v[216:217], v237 offset:0x3600
	ds_read_b64_tr_b16 v[218:219], v237 offset:0x3e00
	s_waitcnt lgkmcnt(8)
	v_mfma_f32_32x32x16_bf16 v[34:49], v[156:159], v[10:13], v[34:49]
	v_mfma_f32_32x32x16_bf16 v[34:49], v[160:163], v[14:17], v[34:49]
	v_mfma_f32_32x32x16_bf16 v[34:49], v[196:199], v[148:151], v[34:49]
	v_mfma_f32_32x32x16_bf16 v[34:49], v[200:203], v[152:155], v[34:49]
	s_waitcnt lgkmcnt(0)
	v_mfma_f32_32x32x16_bf16 v[18:33], v[156:159], v[204:207], v[18:33]
	s_cmp_le_i32 s87, s70
	v_mfma_f32_32x32x16_bf16 v[18:33], v[160:163], v[208:211], v[18:33]
	v_mfma_f32_32x32x16_bf16 v[18:33], v[196:199], v[212:215], v[18:33]
	v_mfma_f32_32x32x16_bf16 v[18:33], v[200:203], v[216:219], v[18:33]
	s_cbranch_scc1 .LBB0_403
	v_cmp_gt_i32_e64 s[60:61], 26, v193
	v_cmp_gt_i32_e64 s[62:63], 27, v193
	v_cmp_gt_i32_e64 s[58:59], 25, v193
	s_and_b64 s[60:61], s[62:63], s[60:61]
	v_cmp_gt_i32_e64 s[56:57], 24, v193
	s_and_b64 s[58:59], s[60:61], s[58:59]
	v_cmp_gt_i32_e64 s[54:55], 19, v193
	s_and_b64 s[56:57], s[58:59], s[56:57]
	v_cmp_gt_i32_e64 s[52:53], 18, v193
	s_and_b64 s[54:55], s[56:57], s[54:55]
	v_cmp_gt_i32_e64 s[50:51], 17, v193
	s_and_b64 s[52:53], s[54:55], s[52:53]
	v_cmp_gt_i32_e64 s[48:49], 16, v193
	s_and_b64 s[50:51], s[52:53], s[50:51]
	v_cmp_gt_i32_e64 s[46:47], 11, v193
	s_and_b64 s[48:49], s[50:51], s[48:49]
	v_cmp_gt_i32_e64 s[44:45], 10, v193
	s_and_b64 s[46:47], s[48:49], s[46:47]
	v_cmp_gt_i32_e64 s[42:43], 9, v193
	s_and_b64 s[44:45], s[46:47], s[44:45]
	v_cmp_gt_i32_e64 s[40:41], 8, v193
	s_and_b64 s[42:43], s[44:45], s[42:43]
	v_cmp_gt_i32_e64 s[38:39], 3, v193
	s_and_b64 s[40:41], s[42:43], s[40:41]
	v_cmp_gt_i32_e64 s[36:37], 2, v193
	s_and_b64 s[38:39], s[40:41], s[38:39]
	v_cmp_gt_i32_e64 s[34:35], 1, v193
	s_and_b64 s[36:37], s[38:39], s[36:37]
	v_cmp_gt_i32_e64 s[30:31], 0, v193
	s_and_b64 s[34:35], s[36:37], s[34:35]
	s_and_b64 s[30:31], s[34:35], s[30:31]
	v_cmp_gt_i32_e64 s[28:29], 58, v193
	v_cndmask_b32_e64 v98, v98, v171, s[30:31]
	v_cmp_gt_i32_e64 s[30:31], 59, v193
	v_cmp_gt_i32_e64 s[26:27], 57, v193
	s_and_b64 s[28:29], s[30:31], s[28:29]
	v_cmp_gt_i32_e64 s[24:25], 56, v193
	s_and_b64 s[26:27], s[28:29], s[26:27]
	v_cmp_gt_i32_e64 s[22:23], 51, v193
	s_and_b64 s[24:25], s[26:27], s[24:25]
	v_cmp_gt_i32_e64 s[20:21], 50, v193
	s_and_b64 s[22:23], s[24:25], s[22:23]
	v_cmp_gt_i32_e64 s[18:19], 49, v193
	s_and_b64 s[20:21], s[22:23], s[20:21]
	v_cmp_gt_i32_e64 s[16:17], 48, v193
	s_and_b64 s[18:19], s[20:21], s[18:19]
	v_cmp_gt_i32_e64 s[14:15], 43, v193
	s_and_b64 s[16:17], s[18:19], s[16:17]
	v_cmp_gt_i32_e64 s[12:13], 42, v193
	s_and_b64 s[14:15], s[16:17], s[14:15]
	v_cmp_gt_i32_e64 s[10:11], 41, v193
	s_and_b64 s[12:13], s[14:15], s[12:13]
	v_cmp_gt_i32_e64 s[8:9], 40, v193
	s_and_b64 s[10:11], s[12:13], s[10:11]
	v_cmp_gt_i32_e64 s[6:7], 35, v193
	s_and_b64 s[8:9], s[10:11], s[8:9]
	v_cmp_gt_i32_e64 s[4:5], 34, v193
	s_and_b64 s[6:7], s[8:9], s[6:7]
	v_cmp_gt_i32_e64 s[2:3], 33, v193
	s_and_b64 s[4:5], s[6:7], s[4:5]
	v_cmp_gt_i32_e32 vcc, 32, v193
	s_and_b64 s[2:3], s[4:5], s[2:3]
	s_and_b64 vcc, s[2:3], vcc
	v_cndmask_b32_e64 v113, v113, v171, s[62:63]
	v_cndmask_b32_e64 v112, v112, v171, s[60:61]
	v_cndmask_b32_e64 v111, v111, v171, s[58:59]
	v_cndmask_b32_e64 v110, v110, v171, s[56:57]
	v_cndmask_b32_e64 v109, v109, v171, s[54:55]
	v_cndmask_b32_e64 v108, v108, v171, s[52:53]
	v_cndmask_b32_e64 v107, v107, v171, s[50:51]
	v_cndmask_b32_e64 v106, v106, v171, s[48:49]
	v_cndmask_b32_e64 v105, v105, v171, s[46:47]
	v_cndmask_b32_e64 v104, v104, v171, s[44:45]
	v_cndmask_b32_e64 v103, v103, v171, s[42:43]
	v_cndmask_b32_e64 v102, v102, v171, s[40:41]
	v_cndmask_b32_e64 v101, v101, v171, s[38:39]
	v_cndmask_b32_e64 v100, v100, v171, s[36:37]
	v_cndmask_b32_e64 v99, v99, v171, s[34:35]
	v_cndmask_b32_e64 v97, v97, v171, s[30:31]
	v_cndmask_b32_e64 v96, v96, v171, s[28:29]
	v_cndmask_b32_e64 v95, v95, v171, s[26:27]
	v_cndmask_b32_e64 v94, v94, v171, s[24:25]
	v_cndmask_b32_e64 v93, v93, v171, s[22:23]
	v_cndmask_b32_e64 v92, v92, v171, s[20:21]
	v_cndmask_b32_e64 v91, v91, v171, s[18:19]
	v_cndmask_b32_e64 v90, v90, v171, s[16:17]
	v_cndmask_b32_e64 v89, v89, v171, s[14:15]
	v_cndmask_b32_e64 v88, v88, v171, s[12:13]
	v_cndmask_b32_e64 v87, v87, v171, s[10:11]
	v_cndmask_b32_e64 v86, v86, v171, s[8:9]
	v_cndmask_b32_e64 v85, v85, v171, s[6:7]
	v_cndmask_b32_e64 v84, v84, v171, s[4:5]
	v_cndmask_b32_e64 v83, v83, v171, s[2:3]
	v_cndmask_b32_e32 v82, v82, v171, vcc
